# first K iteration of each GEMM unit peeled in the in-proj, out-proj, scores and PV loops: first MFMA into each accumulator takes C=0, so the 128 v_mov accumulator zeroing per unit is gone (barrier str
# speedup vs baseline: 1.0142x; 1.0142x over previous
; #define PG8_STAGE_B(b, h, bp) PG8_STAGE2(PG8_SB(b, h), (bp) + (h) * hstepB, voffB[0], voffB[1])
; #define PG8_STAGE_A(b, h, ap, NX) do { if constexpr (GATHER) { const unsigned _o0 = (NX) ? vn[h][0] : vc[h][0], _o1 = (NX) ? vn[h][1] : vc[h][1]; PG8_STAGE2(PG8_SA(b, h), (ap), _o0, _o1); } \
;         else { PG8_STAGE2(PG8_SA(b, h), (ap) + (h) * hstepA, voffA[0], voffA[1]); } } while (0)
; #define PG8_LDA(dst, b, h) do { _Pragma("unroll") for (int m = 0; m < 4; ++m) _Pragma("unroll") for (int k = 0; k < 2; ++k) dst[m][k] = *(const LAS bf16x8*)(lds + PG8_SA(b, h) + aoff + m * 2048 + k * 1024); } while (0)
; #define PG8_LDB(dst, b, h) do { _Pragma("unroll") for (int n = 0; n < 2; ++n) _Pragma("unroll") for (int k = 0; k < 2; ++k) dst[n][k] = *(const LAS bf16x8*)(lds + PG8_SB(b, h) + boff + n * 2048 + k * 1024); } while (0)
; #define PG8_MMA(ai, bj, At, Bt) do { __builtin_amdgcn_s_setprio(1); _Pragma("unroll") for (int m = 0; m < 4; ++m) _Pragma("unroll") for (int n = 0; n < 2; ++n) _Pragma("unroll") for (int k = 0; k < 2; ++k) \
;         acc[ai][bj][m][n] = __builtin_amdgcn_mfma_f32_16x16x32_bf16(Bt[n][k], At[m][k], acc[ai][bj][m][n], 0, 0, 0); __builtin_amdgcn_s_setprio(0); } while (0)
; template <class Epi, class Sched, bool GATHER, bool LIGHTSKIP = false>
; __device__ __forceinline__ void gemm_phase(LAS unsigned char* lds, LAS unsigned char* xl, const int lda, const int ldb, const int K, const Sched& S, const Epi& E) {
;     ...
;         for (int t = 0; t < nt; t += 2) {
;             const bool last = (t == nt - 2);
;             const char* a1 = cA + (size_t)(t + 1) * kstep;
;             const char* a2 = last ? nA : cA + (size_t)(t + 2) * kstep; const char* b2 = last ? nB : cB + (size_t)(t + 2) * kstep;
;             const char* a3 = a2 + kstep; const char* b3 = b2 + kstep;
;             if constexpr (GATHER) { if (last && has_next) S.offsets(nxt, lda, vn); }
;             PG8_LDB(B0, 0, 0); PG8_LDB(B1, 0, 1); PG8_SCHED; PG8_LDA(At, 0, 0); PG8_STAGE_A(1, 1, a1, false);
;             PG8_WAIT_V(8); PG8_WAIT_L(0); PG8_BAR; PG8_MMA(0, 0, At, B0); PG8_MMA(0, 1, At, B1); PG8_BAR; PG8_SCHED;
;             PG8_LDA(At, 0, 1); PG8_STAGE_B(0, 0, b2); PG8_STAGE_B(0, 1, b2); PG8_STAGE_A(0, 0, a2, last);
;             PG8_WAIT_V(8); PG8_WAIT_L(0); PG8_BAR; if (!light) { PG8_MMA(1, 0, At, B0); PG8_MMA(1, 1, At, B1); } PG8_BAR; PG8_SCHED;
.LBB0_153:
	ds_read_b128 v[152:155], v148
	ds_read_b128 v[156:159], v148 offset:1024
	ds_read_b128 v[160:163], v148 offset:2048
	ds_read_b128 v[164:167], v148 offset:3072
	ds_read_b128 v[168:171], v149
	ds_read_b128 v[172:175], v149 offset:1024
	ds_read_b128 v[176:179], v149 offset:2048
	ds_read_b128 v[180:183], v149 offset:3072
	s_add_u32 s28, s22, 0xfff80080
	s_addc_u32 s29, s23, -1
	s_cmp_eq_u32 s47, 28
	s_cselect_b32 s31, s19, s29
	s_cselect_b32 s30, s18, s28
	s_cselect_b32 s29, s21, s46
	s_cselect_b32 s28, s20, s45
	v_lshl_add_u64 v[216:217], s[22:23], 0, v[138:139]
	s_add_i32 m0, s7, 0xc000
	ds_read_b128 v[184:187], v150
	ds_read_b128 v[188:191], v150 offset:1024
	ds_read_b128 v[192:195], v150 offset:2048
	ds_read_b128 v[196:199], v150 offset:3072
	ds_read_b128 v[200:203], v150 offset:4096
	ds_read_b128 v[204:207], v150 offset:5120
	ds_read_b128 v[208:211], v150 offset:6144
	ds_read_b128 v[212:215], v150 offset:7168
	global_load_lds_dwordx4 v[216:217], off
	v_lshl_add_u64 v[216:217], s[22:23], 0, v[140:141]
	s_add_i32 m0, s7, 0xe000
	s_nop 0
	global_load_lds_dwordx4 v[216:217], off
	s_waitcnt vmcnt(8)
	s_waitcnt lgkmcnt(0)
	s_barrier
	s_waitcnt lgkmcnt(0)
	v_mfma_f32_16x16x32_bf16 v[126:129], v[152:155], v[184:187], v[126:129]
	v_mfma_f32_16x16x32_bf16 v[122:125], v[160:163], v[184:187], v[122:125]
	v_mfma_f32_16x16x32_bf16 v[118:121], v[152:155], v[192:195], v[118:121]
	v_mfma_f32_16x16x32_bf16 v[114:117], v[160:163], v[192:195], v[114:117]
	v_mfma_f32_16x16x32_bf16 v[102:105], v[152:155], v[200:203], v[102:105]
	v_mfma_f32_16x16x32_bf16 v[98:101], v[160:163], v[200:203], v[98:101]
	v_mfma_f32_16x16x32_bf16 v[86:89], v[152:155], v[208:211], v[86:89]
	v_mfma_f32_16x16x32_bf16 v[82:85], v[160:163], v[208:211], v[82:85]
	v_mfma_f32_16x16x32_bf16 v[126:129], v[156:159], v[188:191], v[126:129]
	v_mfma_f32_16x16x32_bf16 v[122:125], v[164:167], v[188:191], v[122:125]
	v_mfma_f32_16x16x32_bf16 v[118:121], v[156:159], v[196:199], v[118:121]
	v_mfma_f32_16x16x32_bf16 v[114:117], v[164:167], v[196:199], v[114:117]
	v_mfma_f32_16x16x32_bf16 v[102:105], v[156:159], v[204:207], v[102:105]
	v_mfma_f32_16x16x32_bf16 v[98:101], v[164:167], v[204:207], v[98:101]
	v_mfma_f32_16x16x32_bf16 v[86:89], v[156:159], v[212:215], v[86:89]
	v_mfma_f32_16x16x32_bf16 v[82:85], v[164:167], v[212:215], v[82:85]
	v_mfma_f32_16x16x32_bf16 v[110:113], v[168:171], v[184:187], v[110:113]
	v_mfma_f32_16x16x32_bf16 v[106:109], v[176:179], v[184:187], v[106:109]
	v_mfma_f32_16x16x32_bf16 v[94:97], v[168:171], v[192:195], v[94:97]
	v_mfma_f32_16x16x32_bf16 v[90:93], v[176:179], v[192:195], v[90:93]
	v_mfma_f32_16x16x32_bf16 v[78:81], v[168:171], v[200:203], v[78:81]
	v_mfma_f32_16x16x32_bf16 v[74:77], v[176:179], v[200:203], v[74:77]
	v_mfma_f32_16x16x32_bf16 v[70:73], v[168:171], v[208:211], v[70:73]
	v_mfma_f32_16x16x32_bf16 v[66:69], v[176:179], v[208:211], v[66:69]
	v_mfma_f32_16x16x32_bf16 v[110:113], v[172:175], v[188:191], v[110:113]
	v_mfma_f32_16x16x32_bf16 v[106:109], v[180:183], v[188:191], v[106:109]
	v_mfma_f32_16x16x32_bf16 v[94:97], v[172:175], v[196:199], v[94:97]
	v_mfma_f32_16x16x32_bf16 v[90:93], v[180:183], v[196:199], v[90:93]
	v_mfma_f32_16x16x32_bf16 v[78:81], v[172:175], v[204:207], v[78:81]
	v_mfma_f32_16x16x32_bf16 v[74:77], v[180:183], v[204:207], v[74:77]
	v_mfma_f32_16x16x32_bf16 v[70:73], v[172:175], v[212:215], v[70:73]
	v_mfma_f32_16x16x32_bf16 v[66:69], v[180:183], v[212:215], v[66:69]
	s_barrier
	s_add_i32 s48, s38, s4
	v_lshl_add_u64 v[216:217], s[28:29], 0, v[134:135]
	s_mov_b32 m0, s48
	ds_read_b128 v[184:187], v150 offset:16384
	ds_read_b128 v[188:191], v150 offset:17408
	ds_read_b128 v[192:195], v150 offset:18432
	ds_read_b128 v[196:199], v150 offset:19456
	ds_read_b128 v[200:203], v150 offset:20480
	ds_read_b128 v[204:207], v150 offset:21504
	ds_read_b128 v[208:211], v150 offset:22528
	ds_read_b128 v[212:215], v150 offset:23552
	global_load_lds_dwordx4 v[216:217], off
	s_add_i32 m0, s48, 0x2000
	s_add_u32 s48, s28, 0x80000
	v_lshl_add_u64 v[218:219], s[28:29], 0, v[130:131]
	s_addc_u32 s49, s29, 0
	s_add_i32 s50, s39, s4
	global_load_lds_dwordx4 v[218:219], off
	v_lshl_add_u64 v[220:221], s[48:49], 0, v[134:135]
	s_mov_b32 m0, s50
	v_lshl_add_u64 v[222:223], s[30:31], 0, v[132:133]
	global_load_lds_dwordx4 v[220:221], off
	v_lshl_add_u64 v[220:221], s[48:49], 0, v[130:131]
	s_add_i32 m0, s50, 0x2000
	s_nop 0
	global_load_lds_dwordx4 v[220:221], off
	v_lshl_add_u64 v[220:221], s[30:31], 0, v[136:137]
	s_mov_b32 m0, s7
	s_nop 0
	global_load_lds_dwordx4 v[220:221], off
	s_mov_b32 m0, s26
	s_nop 0
	global_load_lds_dwordx4 v[222:223], off
	s_waitcnt vmcnt(8)
	s_waitcnt lgkmcnt(0)
	s_barrier
; #define PG8_STAGE_A(b, h, ap, NX) do { if constexpr (GATHER) { const unsigned _o0 = (NX) ? vn[h][0] : vc[h][0], _o1 = (NX) ? vn[h][1] : vc[h][1]; PG8_STAGE2(PG8_SA(b, h), (ap), _o0, _o1); } \
;         else { PG8_STAGE2(PG8_SA(b, h), (ap) + (h) * hstepA, voffA[0], voffA[1]); } } while (0)
; #define PG8_LDA(dst, b, h) do { _Pragma("unroll") for (int m = 0; m < 4; ++m) _Pragma("unroll") for (int k = 0; k < 2; ++k) dst[m][k] = *(const LAS bf16x8*)(lds + PG8_SA(b, h) + aoff + m * 2048 + k * 1024); } while (0)
; #define PG8_LDB(dst, b, h) do { _Pragma("unroll") for (int n = 0; n < 2; ++n) _Pragma("unroll") for (int k = 0; k < 2; ++k) dst[n][k] = *(const LAS bf16x8*)(lds + PG8_SB(b, h) + boff + n * 2048 + k * 1024); } while (0)
; #define PG8_MMA(ai, bj, At, Bt) do { __builtin_amdgcn_s_setprio(1); _Pragma("unroll") for (int m = 0; m < 4; ++m) _Pragma("unroll") for (int n = 0; n < 2; ++n) _Pragma("unroll") for (int k = 0; k < 2; ++k) \
;         acc[ai][bj][m][n] = __builtin_amdgcn_mfma_f32_16x16x32_bf16(Bt[n][k], At[m][k], acc[ai][bj][m][n], 0, 0, 0); __builtin_amdgcn_s_setprio(0); } while (0)
; #define PG8_WAIT_V(n) asm volatile("s_waitcnt vmcnt(" #n ")" ::: "memory")
; #define PG8_WAIT_L(n) asm volatile("s_waitcnt lgkmcnt(" #n ")" ::: "memory")
; #define PG8_BAR __builtin_amdgcn_s_barrier()
; #define PG8_SCHED __builtin_amdgcn_sched_barrier(0)
; template <class Epi, class Sched, bool GATHER, bool LIGHTSKIP = false>
; __device__ __forceinline__ void gemm_phase(LAS unsigned char* lds, LAS unsigned char* xl, const int lda, const int ldb, const int K, const Sched& S, const Epi& E) {
;     ...
;             PG8_WAIT_V(8); PG8_WAIT_L(0); PG8_BAR; if (!light) { PG8_MMA(1, 0, At, B0); PG8_MMA(1, 1, At, B1); } PG8_BAR; PG8_SCHED;
;             PG8_LDB(B0, 1, 0); PG8_LDB(B1, 1, 1); PG8_SCHED; PG8_LDA(At, 1, 0); PG8_STAGE_A(0, 1, a2, last);
;             PG8_WAIT_V(8); PG8_WAIT_L(0); PG8_BAR; PG8_MMA(0, 0, At, B0); PG8_MMA(0, 1, At, B1); PG8_BAR; PG8_SCHED;
	s_waitcnt lgkmcnt(0)
	v_mfma_f32_16x16x32_bf16 v[62:65], v[152:155], v[184:187], v[62:65]
	v_mfma_f32_16x16x32_bf16 v[58:61], v[160:163], v[184:187], v[58:61]
	v_mfma_f32_16x16x32_bf16 v[54:57], v[152:155], v[192:195], v[54:57]
	v_mfma_f32_16x16x32_bf16 v[50:53], v[160:163], v[192:195], v[50:53]
	v_mfma_f32_16x16x32_bf16 v[38:41], v[152:155], v[200:203], v[38:41]
	v_mfma_f32_16x16x32_bf16 v[34:37], v[160:163], v[200:203], v[34:37]
	v_mfma_f32_16x16x32_bf16 v[22:25], v[152:155], v[208:211], v[22:25]
	v_mfma_f32_16x16x32_bf16 v[18:21], v[160:163], v[208:211], v[18:21]
	v_mfma_f32_16x16x32_bf16 v[62:65], v[156:159], v[188:191], v[62:65]
	v_mfma_f32_16x16x32_bf16 v[58:61], v[164:167], v[188:191], v[58:61]
	v_mfma_f32_16x16x32_bf16 v[54:57], v[156:159], v[196:199], v[54:57]
	v_mfma_f32_16x16x32_bf16 v[50:53], v[164:167], v[196:199], v[50:53]
	v_mfma_f32_16x16x32_bf16 v[38:41], v[156:159], v[204:207], v[38:41]
	v_mfma_f32_16x16x32_bf16 v[34:37], v[164:167], v[204:207], v[34:37]
	v_mfma_f32_16x16x32_bf16 v[22:25], v[156:159], v[212:215], v[22:25]
	v_mfma_f32_16x16x32_bf16 v[18:21], v[164:167], v[212:215], v[18:21]
	v_mfma_f32_16x16x32_bf16 v[46:49], v[168:171], v[184:187], v[46:49]
	v_mfma_f32_16x16x32_bf16 v[42:45], v[176:179], v[184:187], v[42:45]
	v_mfma_f32_16x16x32_bf16 v[30:33], v[168:171], v[192:195], v[30:33]
	v_mfma_f32_16x16x32_bf16 v[26:29], v[176:179], v[192:195], v[26:29]
	v_mfma_f32_16x16x32_bf16 v[14:17], v[168:171], v[200:203], v[14:17]
	v_mfma_f32_16x16x32_bf16 v[10:13], v[176:179], v[200:203], v[10:13]
	v_mfma_f32_16x16x32_bf16 v[6:9], v[168:171], v[208:211], v[6:9]
	v_mfma_f32_16x16x32_bf16 v[2:5], v[176:179], v[208:211], v[2:5]
	v_mfma_f32_16x16x32_bf16 v[46:49], v[172:175], v[188:191], v[46:49]
	v_mfma_f32_16x16x32_bf16 v[42:45], v[180:183], v[188:191], v[42:45]
	v_mfma_f32_16x16x32_bf16 v[30:33], v[172:175], v[196:199], v[30:33]
	v_mfma_f32_16x16x32_bf16 v[26:29], v[180:183], v[196:199], v[26:29]
	v_mfma_f32_16x16x32_bf16 v[14:17], v[172:175], v[204:207], v[14:17]
	v_mfma_f32_16x16x32_bf16 v[10:13], v[180:183], v[204:207], v[10:13]
	v_mfma_f32_16x16x32_bf16 v[6:9], v[172:175], v[212:215], v[6:9]
	v_mfma_f32_16x16x32_bf16 v[2:5], v[180:183], v[212:215], v[2:5]
	s_barrier
	s_add_i32 s48, 0, 0x18000
	v_add_u32_e32 v151, s48, v146
	s_add_i32 s49, 0, 0x1c000
	ds_read_b128 v[152:155], v151
	ds_read_b128 v[156:159], v151 offset:1024
	ds_read_b128 v[160:163], v151 offset:2048
	ds_read_b128 v[164:167], v151 offset:3072
	v_add_u32_e32 v151, s49, v146
	ds_read_b128 v[168:171], v151
	ds_read_b128 v[172:175], v151 offset:1024
	ds_read_b128 v[176:179], v151 offset:2048
	ds_read_b128 v[180:183], v151 offset:3072
	s_add_u32 s30, s30, 0x80000
	s_addc_u32 s31, s31, 0
	s_mov_b32 m0, s27
	v_lshl_add_u64 v[224:225], s[30:31], 0, v[136:137]
	ds_read_b128 v[184:187], v150 offset:32768
	ds_read_b128 v[188:191], v150 offset:33792
	ds_read_b128 v[192:195], v150 offset:34816
	ds_read_b128 v[196:199], v150 offset:35840
	ds_read_b128 v[200:203], v150 offset:36864
	ds_read_b128 v[204:207], v150 offset:37888
	ds_read_b128 v[208:211], v150 offset:38912
	ds_read_b128 v[212:215], v150 offset:39936
	global_load_lds_dwordx4 v[224:225], off
	v_lshl_add_u64 v[224:225], s[30:31], 0, v[132:133]
	s_mov_b32 m0, s33
	s_nop 0
	global_load_lds_dwordx4 v[224:225], off
	s_waitcnt vmcnt(8)
	s_waitcnt lgkmcnt(0)
	s_barrier
	s_waitcnt lgkmcnt(0)
	v_mfma_f32_16x16x32_bf16 v[126:129], v[152:155], v[184:187], v[126:129]
	v_mfma_f32_16x16x32_bf16 v[122:125], v[160:163], v[184:187], v[122:125]
	v_mfma_f32_16x16x32_bf16 v[118:121], v[152:155], v[192:195], v[118:121]
	v_mfma_f32_16x16x32_bf16 v[114:117], v[160:163], v[192:195], v[114:117]
	v_mfma_f32_16x16x32_bf16 v[102:105], v[152:155], v[200:203], v[102:105]
	v_mfma_f32_16x16x32_bf16 v[98:101], v[160:163], v[200:203], v[98:101]
	v_mfma_f32_16x16x32_bf16 v[86:89], v[152:155], v[208:211], v[86:89]
	v_mfma_f32_16x16x32_bf16 v[82:85], v[160:163], v[208:211], v[82:85]
	v_mfma_f32_16x16x32_bf16 v[126:129], v[156:159], v[188:191], v[126:129]
	v_mfma_f32_16x16x32_bf16 v[122:125], v[164:167], v[188:191], v[122:125]
	v_mfma_f32_16x16x32_bf16 v[118:121], v[156:159], v[196:199], v[118:121]
	v_mfma_f32_16x16x32_bf16 v[114:117], v[164:167], v[196:199], v[114:117]
	v_mfma_f32_16x16x32_bf16 v[102:105], v[156:159], v[204:207], v[102:105]
	v_mfma_f32_16x16x32_bf16 v[98:101], v[164:167], v[204:207], v[98:101]
	v_mfma_f32_16x16x32_bf16 v[86:89], v[156:159], v[212:215], v[86:89]
	v_mfma_f32_16x16x32_bf16 v[82:85], v[164:167], v[212:215], v[82:85]
	v_mfma_f32_16x16x32_bf16 v[110:113], v[168:171], v[184:187], v[110:113]
	v_mfma_f32_16x16x32_bf16 v[106:109], v[176:179], v[184:187], v[106:109]
	v_mfma_f32_16x16x32_bf16 v[94:97], v[168:171], v[192:195], v[94:97]
	v_mfma_f32_16x16x32_bf16 v[90:93], v[176:179], v[192:195], v[90:93]
	v_mfma_f32_16x16x32_bf16 v[78:81], v[168:171], v[200:203], v[78:81]
	v_mfma_f32_16x16x32_bf16 v[74:77], v[176:179], v[200:203], v[74:77]
	v_mfma_f32_16x16x32_bf16 v[70:73], v[168:171], v[208:211], v[70:73]
	v_mfma_f32_16x16x32_bf16 v[66:69], v[176:179], v[208:211], v[66:69]
	v_mfma_f32_16x16x32_bf16 v[110:113], v[172:175], v[188:191], v[110:113]
	v_mfma_f32_16x16x32_bf16 v[106:109], v[180:183], v[188:191], v[106:109]
	v_mfma_f32_16x16x32_bf16 v[94:97], v[172:175], v[196:199], v[94:97]
	v_mfma_f32_16x16x32_bf16 v[90:93], v[180:183], v[196:199], v[90:93]
	v_mfma_f32_16x16x32_bf16 v[78:81], v[172:175], v[204:207], v[78:81]
	v_mfma_f32_16x16x32_bf16 v[74:77], v[180:183], v[204:207], v[74:77]
	v_mfma_f32_16x16x32_bf16 v[70:73], v[172:175], v[212:215], v[70:73]
	v_mfma_f32_16x16x32_bf16 v[66:69], v[180:183], v[212:215], v[66:69]
	s_barrier
; #define PG8_STAGE_B(b, h, bp) PG8_STAGE2(PG8_SB(b, h), (bp) + (h) * hstepB, voffB[0], voffB[1])
; #define PG8_STAGE_A(b, h, ap, NX) do { if constexpr (GATHER) { const unsigned _o0 = (NX) ? vn[h][0] : vc[h][0], _o1 = (NX) ? vn[h][1] : vc[h][1]; PG8_STAGE2(PG8_SA(b, h), (ap), _o0, _o1); } \
;         else { PG8_STAGE2(PG8_SA(b, h), (ap) + (h) * hstepA, voffA[0], voffA[1]); } } while (0)
; #define PG8_LDA(dst, b, h) do { _Pragma("unroll") for (int m = 0; m < 4; ++m) _Pragma("unroll") for (int k = 0; k < 2; ++k) dst[m][k] = *(const LAS bf16x8*)(lds + PG8_SA(b, h) + aoff + m * 2048 + k * 1024); } while (0)
; #define PG8_MMA(ai, bj, At, Bt) do { __builtin_amdgcn_s_setprio(1); _Pragma("unroll") for (int m = 0; m < 4; ++m) _Pragma("unroll") for (int n = 0; n < 2; ++n) _Pragma("unroll") for (int k = 0; k < 2; ++k) \
;         acc[ai][bj][m][n] = __builtin_amdgcn_mfma_f32_16x16x32_bf16(Bt[n][k], At[m][k], acc[ai][bj][m][n], 0, 0, 0); __builtin_amdgcn_s_setprio(0); } while (0)
; #define PG8_WAIT_V(n) asm volatile("s_waitcnt vmcnt(" #n ")" ::: "memory")
; #define PG8_WAIT_L(n) asm volatile("s_waitcnt lgkmcnt(" #n ")" ::: "memory")
; #define PG8_BAR __builtin_amdgcn_s_barrier()
; #define PG8_SCHED __builtin_amdgcn_sched_barrier(0)
; template <class Epi, class Sched, bool GATHER, bool LIGHTSKIP = false>
; __device__ __forceinline__ void gemm_phase(LAS unsigned char* lds, LAS unsigned char* xl, const int lda, const int ldb, const int K, const Sched& S, const Epi& E) {
;     ...
;             PG8_LDA(At, 1, 1); PG8_STAGE_B(1, 0, b3); PG8_STAGE_B(1, 1, b3); PG8_STAGE_A(1, 0, a3, last);
;             PG8_WAIT_V(8); PG8_WAIT_L(0); PG8_BAR; if (!light) { PG8_MMA(1, 0, At, B0); PG8_MMA(1, 1, At, B1); } PG8_BAR; PG8_SCHED;
;         }
;         if (wr == 0) PG8_BAR;
	s_add_i32 s30, s48, s4
	v_lshl_add_u64 v[216:217], v[216:217], 0, s[14:15]
	s_mov_b32 m0, s30
	ds_read_b128 v[184:187], v150 offset:49152
	ds_read_b128 v[188:191], v150 offset:50176
	ds_read_b128 v[192:195], v150 offset:51200
	ds_read_b128 v[196:199], v150 offset:52224
	ds_read_b128 v[200:203], v150 offset:53248
	ds_read_b128 v[204:207], v150 offset:54272
	ds_read_b128 v[208:211], v150 offset:55296
	ds_read_b128 v[212:215], v150 offset:56320
	global_load_lds_dwordx4 v[216:217], off
	s_add_i32 m0, s30, 0x2000
	s_add_u32 s28, s28, 0x80080
	v_lshl_add_u64 v[216:217], v[218:219], 0, s[14:15]
	s_addc_u32 s29, s29, 0
	s_add_i32 s30, s49, s4
	global_load_lds_dwordx4 v[216:217], off
	v_lshl_add_u64 v[216:217], s[28:29], 0, v[134:135]
	s_mov_b32 m0, s30
	s_nop 0
	global_load_lds_dwordx4 v[216:217], off
	v_lshl_add_u64 v[216:217], s[28:29], 0, v[130:131]
	s_add_i32 m0, s30, 0x2000
	s_nop 0
	global_load_lds_dwordx4 v[216:217], off
	v_lshl_add_u64 v[216:217], v[220:221], 0, s[14:15]
	s_mov_b32 m0, s35
	s_nop 0
	global_load_lds_dwordx4 v[216:217], off
	v_lshl_add_u64 v[216:217], v[222:223], 0, s[14:15]
	s_mov_b32 m0, s36
	s_nop 0
	global_load_lds_dwordx4 v[216:217], off
	s_waitcnt vmcnt(8)
	s_waitcnt lgkmcnt(0)
	s_barrier
	s_waitcnt lgkmcnt(0)
	v_mfma_f32_16x16x32_bf16 v[62:65], v[152:155], v[184:187], v[62:65]
	v_mfma_f32_16x16x32_bf16 v[58:61], v[160:163], v[184:187], v[58:61]
	v_mfma_f32_16x16x32_bf16 v[54:57], v[152:155], v[192:195], v[54:57]
	v_mfma_f32_16x16x32_bf16 v[50:53], v[160:163], v[192:195], v[50:53]
	v_mfma_f32_16x16x32_bf16 v[38:41], v[152:155], v[200:203], v[38:41]
	v_mfma_f32_16x16x32_bf16 v[34:37], v[160:163], v[200:203], v[34:37]
	v_mfma_f32_16x16x32_bf16 v[22:25], v[152:155], v[208:211], v[22:25]
	v_mfma_f32_16x16x32_bf16 v[18:21], v[160:163], v[208:211], v[18:21]
	v_mfma_f32_16x16x32_bf16 v[62:65], v[156:159], v[188:191], v[62:65]
	v_mfma_f32_16x16x32_bf16 v[58:61], v[164:167], v[188:191], v[58:61]
	v_mfma_f32_16x16x32_bf16 v[54:57], v[156:159], v[196:199], v[54:57]
	v_mfma_f32_16x16x32_bf16 v[50:53], v[164:167], v[196:199], v[50:53]
	v_mfma_f32_16x16x32_bf16 v[38:41], v[156:159], v[204:207], v[38:41]
	v_mfma_f32_16x16x32_bf16 v[34:37], v[164:167], v[204:207], v[34:37]
	v_mfma_f32_16x16x32_bf16 v[22:25], v[156:159], v[212:215], v[22:25]
	v_mfma_f32_16x16x32_bf16 v[18:21], v[164:167], v[212:215], v[18:21]
	v_mfma_f32_16x16x32_bf16 v[46:49], v[168:171], v[184:187], v[46:49]
	v_mfma_f32_16x16x32_bf16 v[42:45], v[176:179], v[184:187], v[42:45]
	v_mfma_f32_16x16x32_bf16 v[30:33], v[168:171], v[192:195], v[30:33]
	v_mfma_f32_16x16x32_bf16 v[26:29], v[176:179], v[192:195], v[26:29]
	v_mfma_f32_16x16x32_bf16 v[14:17], v[168:171], v[200:203], v[14:17]
	v_mfma_f32_16x16x32_bf16 v[10:13], v[176:179], v[200:203], v[10:13]
	v_mfma_f32_16x16x32_bf16 v[6:9], v[168:171], v[208:211], v[6:9]
	v_mfma_f32_16x16x32_bf16 v[2:5], v[176:179], v[208:211], v[2:5]
	v_mfma_f32_16x16x32_bf16 v[46:49], v[172:175], v[188:191], v[46:49]
	v_mfma_f32_16x16x32_bf16 v[42:45], v[180:183], v[188:191], v[42:45]
	v_mfma_f32_16x16x32_bf16 v[30:33], v[172:175], v[196:199], v[30:33]
	v_mfma_f32_16x16x32_bf16 v[26:29], v[180:183], v[196:199], v[26:29]
	v_mfma_f32_16x16x32_bf16 v[14:17], v[172:175], v[204:207], v[14:17]
	v_mfma_f32_16x16x32_bf16 v[10:13], v[180:183], v[204:207], v[10:13]
	v_mfma_f32_16x16x32_bf16 v[6:9], v[172:175], v[212:215], v[6:9]
	v_mfma_f32_16x16x32_bf16 v[2:5], v[180:183], v[212:215], v[2:5]
	s_barrier
	s_add_i32 s47, s47, 2
	s_add_u32 s22, s22, 0x100
	s_addc_u32 s23, s23, 0
	s_add_u32 s45, s45, 0x100
	s_addc_u32 s46, s46, 0
	s_cmp_gt_u32 s47, 29
	s_cbranch_scc0 .LBB0_153
.Lpeel_exit_0:
	s_and_b64 vcc, exec, s[16:17]
	s_cbranch_vccz .LBB0_156
	s_barrier
